# P9 norm: 20 v_pk_fma_f32 fed by single-use v_mov copies split into plain v_fma_f32 on the original registers (28 fewer VALU per 2 tokens)
# baseline (speedup 1.0000x reference)
; #define LAS __attribute__((address_space(3)))
; __device__ __forceinline__ unsigned pk2(float lo, float hi) { return f2bf(lo) | (f2bf(hi) << 16); }
; __device__ __forceinline__ void norm_mod_regs_lds2(const u32x4 (&w)[4], const LAS float* A, const LAS float* B, LAS unsigned char* lrow, int sw, unsigned char* o8row, int lane) {
;     float s = 0.f;
; #pragma unroll
;     for (int j = 0; j < 4; ++j) {
; #pragma unroll
;         for (int i = 0; i < 4; ++i) { const float a = bf_lo(w[j][i]), b = bf_hi(w[j][i]); s += a * a + b * b; } }
;     const float rstd = 1.f / sqrtf(wave_sum(s) * (1.f / DM) + EPS_);
;     const unsigned l8 = (unsigned)lane * 8u;
; #pragma unroll
;     for (int j = 0; j < 4; ++j) {
;         const f32x4 a0 = *(const LAS f32x4*)(A + 512 * j + 8 * lane), a1 = *(const LAS f32x4*)(A + 512 * j + 8 * lane + 4), b0 = *(const LAS f32x4*)(B + 512 * j + 8 * lane), b1 = *(const LAS f32x4*)(B + 512 * j + 8 * lane + 4);
;         const f32x4 h0 = {bf_lo(w[j][0]) * rstd * a0[0] + b0[0], bf_hi(w[j][0]) * rstd * a0[1] + b0[1], bf_lo(w[j][1]) * rstd * a0[2] + b0[2], bf_hi(w[j][1]) * rstd * a0[3] + b0[3]};
;         const f32x4 h1 = {bf_lo(w[j][2]) * rstd * a1[0] + b1[0], bf_hi(w[j][2]) * rstd * a1[1] + b1[1], bf_lo(w[j][3]) * rstd * a1[2] + b1[2], bf_hi(w[j][3]) * rstd * a1[3] + b1[3]};
;         u32x4 o; o.x = pk2(h0[0], h0[1]); o.y = pk2(h0[2], h0[3]); o.z = pk2(h1[0], h1[1]); o.w = pk2(h1[2], h1[3]);
;         *(LAS u32x4*)(lrow + (((lane + 64 * j) ^ sw) << 4)) = o;
;         u32x2 q8; q8.x = pg8::pack4_fp8(h0, pg8::F8_SH); q8.y = pg8::pack4_fp8(h1, pg8::F8_SH); *(u32x2*)((char*)(o8row + 512 * j) + l8) = q8;
.LBB0_1399:
	s_waitcnt vmcnt(7)
	v_and_b32_e32 v233, 0xffff0000, v115
	v_and_b32_e32 v232, 0xffff0000, v114
	v_lshlrev_b32_e32 v231, 16, v115
	v_lshlrev_b32_e32 v230, 16, v114
	v_pk_mul_f32 v[152:153], v[232:233], v[232:233]
	v_and_b32_e32 v237, 0xffff0000, v117
	v_and_b32_e32 v236, 0xffff0000, v116
	v_pk_fma_f32 v[160:161], v[230:231], v[230:231], v[152:153]
	v_lshlrev_b32_e32 v235, 16, v117
	v_lshlrev_b32_e32 v234, 16, v116
	v_pk_mul_f32 v[152:153], v[236:237], v[236:237]
	s_waitcnt vmcnt(6)
	v_and_b32_e32 v241, 0xffff0000, v119
	v_pk_fma_f32 v[214:215], v[234:235], v[234:235], v[152:153]
	v_and_b32_e32 v240, 0xffff0000, v118
	v_add_f32_e32 v160, v160, v161
	v_lshlrev_b32_e32 v239, 16, v119
	v_lshlrev_b32_e32 v238, 16, v118
	v_pk_mul_f32 v[152:153], v[240:241], v[240:241]
	v_add_f32_e32 v160, v214, v160
	v_pk_fma_f32 v[216:217], v[238:239], v[238:239], v[152:153]
	v_and_b32_e32 v245, 0xffff0000, v121
	v_and_b32_e32 v244, 0xffff0000, v120
	v_add_f32_e32 v160, v215, v160
	v_lshlrev_b32_e32 v243, 16, v121
	v_lshlrev_b32_e32 v242, 16, v120
	v_pk_mul_f32 v[152:153], v[244:245], v[244:245]
	v_add_f32_e32 v160, v216, v160
	v_pk_fma_f32 v[218:219], v[242:243], v[242:243], v[152:153]
	s_waitcnt vmcnt(5)
	v_and_b32_e32 v179, 0xffff0000, v123
	v_and_b32_e32 v178, 0xffff0000, v122
	v_add_f32_e32 v160, v217, v160
	v_lshlrev_b32_e32 v181, 16, v123
	v_lshlrev_b32_e32 v180, 16, v122
	v_pk_mul_f32 v[152:153], v[178:179], v[178:179]
	v_add_f32_e32 v160, v218, v160
	v_pk_fma_f32 v[220:221], v[180:181], v[180:181], v[152:153]
	v_and_b32_e32 v157, 0xffff0000, v125
	v_and_b32_e32 v156, 0xffff0000, v124
	v_add_f32_e32 v160, v219, v160
	v_lshlrev_b32_e32 v159, 16, v125
	v_lshlrev_b32_e32 v158, 16, v124
	v_pk_mul_f32 v[152:153], v[156:157], v[156:157]
	v_add_f32_e32 v160, v220, v160
	v_pk_fma_f32 v[222:223], v[158:159], v[158:159], v[152:153]
	s_waitcnt vmcnt(4)
	v_and_b32_e32 v153, 0xffff0000, v127
	v_and_b32_e32 v152, 0xffff0000, v126
	v_add_f32_e32 v160, v221, v160
	v_lshlrev_b32_e32 v155, 16, v127
	v_lshlrev_b32_e32 v154, 16, v126
	v_pk_mul_f32 v[224:225], v[152:153], v[152:153]
	v_add_f32_e32 v160, v222, v160
	v_and_b32_e32 v147, 0xffff0000, v129
	v_and_b32_e32 v146, 0xffff0000, v128
	v_pk_fma_f32 v[224:225], v[154:155], v[154:155], v[224:225]
	v_add_f32_e32 v160, v223, v160
	v_lshlrev_b32_e32 v149, 16, v129
	v_lshlrev_b32_e32 v148, 16, v128
	v_pk_mul_f32 v[150:151], v[146:147], v[146:147]
	v_add_f32_e32 v160, v224, v160
	v_pk_fma_f32 v[150:151], v[148:149], v[148:149], v[150:151]
	v_add_f32_e32 v160, v225, v160
	v_add_f32_e32 v150, v150, v160
	v_add_f32_e32 v150, v151, v150
	ds_bpermute_b32 v151, v183, v150
	s_add_i32 s24, s40, s27
	s_ashr_i32 s25, s24, 31
	s_lshl_b64 s[22:23], s[24:25], 11
	ds_read_b128 v[214:217], v189
	ds_read_b128 v[218:221], v189 offset:16
	s_waitcnt lgkmcnt(2)
	v_add_f32_e32 v150, v150, v151
	ds_bpermute_b32 v151, v184, v150
	ds_read_b128 v[222:225], v190
	ds_read_b128 v[226:229], v190 offset:16
	s_waitcnt lgkmcnt(4)
	v_mov_b32_e32 v246, v214
	s_waitcnt lgkmcnt(3)
	v_mov_b32_e32 v214, v218
	v_mov_b32_e32 v247, v216
	s_waitcnt lgkmcnt(2)
	v_add_f32_e32 v150, v150, v151
	ds_bpermute_b32 v151, v185, v150
	v_mov_b32_e32 v216, v215
	v_mov_b32_e32 v215, v220
	v_mov_b32_e32 v220, v219
	s_waitcnt lgkmcnt(2)
	v_mov_b32_e32 v248, v222
	s_waitcnt lgkmcnt(0)
	v_add_f32_e32 v160, v150, v151
	ds_bpermute_b32 v161, v186, v160
	v_lshl_add_u64 v[150:151], v[176:177], 0, s[22:23]
	v_mov_b32_e32 v249, v224
	v_mov_b32_e32 v224, v223
	v_mov_b32_e32 v222, v226
	s_waitcnt lgkmcnt(0)
	v_add_f32_e32 v160, v160, v161
	ds_bpermute_b32 v161, v187, v160
	v_mov_b32_e32 v223, v228
	v_mov_b32_e32 v228, v227
	s_waitcnt lgkmcnt(0)
	v_add_f32_e32 v160, v160, v161
	ds_bpermute_b32 v161, v188, v160
	s_waitcnt lgkmcnt(0)
	v_add_f32_e32 v160, v160, v161
	v_fmamk_f32 v160, v160, 0x3a000000, v195
	v_mul_f32_e32 v161, 0x4f800000, v160
	v_cmp_gt_f32_e32 vcc, s53, v160
	s_nop 1
	v_cndmask_b32_e32 v160, v160, v161, vcc
	v_sqrt_f32_e32 v161, v160
	s_nop 0
	v_add_u32_e32 v164, -1, v161
	v_fma_f32 v213, -v164, v161, v160
	v_cmp_ge_f32_e64 s[22:23], 0, v213
	v_add_u32_e32 v213, 1, v161
	s_nop 0
	v_cndmask_b32_e64 v164, v161, v164, s[22:23]
	v_fma_f32 v161, -v213, v161, v160
	v_cmp_lt_f32_e64 s[22:23], 0, v161
	s_nop 1
	v_cndmask_b32_e64 v161, v164, v213, s[22:23]
	v_mul_f32_e32 v164, 0x37800000, v161
	v_cndmask_b32_e32 v161, v161, v164, vcc
	v_cmp_class_f32_e32 vcc, v160, v196
	s_nop 1
	v_cndmask_b32_e32 v160, v161, v160, vcc
	v_div_scale_f32 v161, s[22:23], v160, v160, 1.0
	v_rcp_f32_e32 v164, v161
	s_nop 0
	v_fma_f32 v213, -v161, v164, 1.0
	v_fmac_f32_e32 v164, v213, v164
	v_div_scale_f32 v213, vcc, 1.0, v160, 1.0
	v_mul_f32_e32 v218, v213, v164
	v_fma_f32 v219, -v161, v218, v213
	v_fmac_f32_e32 v218, v219, v164
	v_fma_f32 v161, -v161, v218, v213
	v_div_fmas_f32 v161, v161, v164, v218
	v_div_fixup_f32 v160, v161, v160, 1.0
	v_pk_mul_f32 v[226:227], v[160:161], v[232:233] op_sel_hi:[0,1]
	v_pk_fma_f32 v[224:225], v[216:217], v[226:227], v[224:225]
	v_pk_mul_f32 v[216:217], v[160:161], v[234:235] op_sel_hi:[0,1]
	v_pk_mul_f32 v[218:219], v[160:161], v[230:231] op_sel_hi:[0,1]
	v_pk_fma_f32 v[214:215], v[214:215], v[216:217], v[222:223]
	v_pk_mul_f32 v[216:217], v[160:161], v[236:237] op_sel_hi:[0,1]
	v_pk_fma_f32 v[218:219], v[246:247], v[218:219], v[248:249]
	v_pk_fma_f32 v[220:221], v[220:221], v[216:217], v[228:229]
	v_bfe_u32 v216, v224, 16, 1
	v_add3_u32 v222, v224, v216, s54
	v_bfe_u32 v216, v218, 16, 1
	v_bfe_u32 v217, v219, 16, 1
	v_add3_u32 v217, v219, v217, s54
	v_add3_u32 v216, v218, v216, s54
	v_lshrrev_b32_e32 v227, 16, v216
	v_lshrrev_b32_e32 v228, 16, v217
	v_cvt_pk_bf16_f32 v217, v215, v221
	v_cvt_pk_bf16_f32 v216, v214, v220
	v_med3_f32 v161, v218, s55, v210
	v_med3_f32 v164, v224, s55, v210
	v_mov_b32_e32 v218, 0
	v_cvt_pk_fp8_f32 v218, v161, v164
	v_med3_f32 v161, v219, s55, v210
	v_med3_f32 v214, v214, s55, v210
	v_med3_f32 v220, v220, s55, v210
	v_mov_b32_e32 v219, 0
	v_cvt_pk_fp8_f32 v219, v214, v220
	v_med3_f32 v164, v225, s55, v210
	v_cvt_pk_fp8_f32 v218, v161, v164 op_sel:[0,0,1]
	v_med3_f32 v161, v215, s55, v210
	v_med3_f32 v164, v221, s55, v210
	v_cvt_pk_fp8_f32 v219, v161, v164 op_sel:[0,0,1]
	v_bfe_u32 v213, v225, 16, 1
	v_add3_u32 v213, v225, v213, s54
	v_and_or_b32 v215, v213, s52, v228
	v_and_or_b32 v214, v222, s52, v227
	ds_write_b128 v197, v[214:217]
	global_store_dwordx2 v[150:151], v[218:219], off
	ds_read_b128 v[214:217], v189 offset:2048
	ds_read_b128 v[218:221], v189 offset:2064
	ds_read_b128 v[222:225], v190 offset:2048
	ds_read_b128 v[226:229], v190 offset:2064
	v_pk_mul_f32 v[230:231], v[160:161], v[238:239] op_sel_hi:[0,1]
	s_waitcnt lgkmcnt(3)
; #define LAS __attribute__((address_space(3)))
; __device__ __forceinline__ unsigned pk2(float lo, float hi) { return f2bf(lo) | (f2bf(hi) << 16); }
; __device__ __forceinline__ void norm_mod_regs_lds2(const u32x4 (&w)[4], const LAS float* A, const LAS float* B, LAS unsigned char* lrow, int sw, unsigned char* o8row, int lane) {
;     float s = 0.f;
; #pragma unroll
;     for (int j = 0; j < 4; ++j) {
; #pragma unroll
;         for (int i = 0; i < 4; ++i) { const float a = bf_lo(w[j][i]), b = bf_hi(w[j][i]); s += a * a + b * b; } }
;     const float rstd = 1.f / sqrtf(wave_sum(s) * (1.f / DM) + EPS_);
;     const unsigned l8 = (unsigned)lane * 8u;
; #pragma unroll
;     for (int j = 0; j < 4; ++j) {
;         const f32x4 a0 = *(const LAS f32x4*)(A + 512 * j + 8 * lane), a1 = *(const LAS f32x4*)(A + 512 * j + 8 * lane + 4), b0 = *(const LAS f32x4*)(B + 512 * j + 8 * lane), b1 = *(const LAS f32x4*)(B + 512 * j + 8 * lane + 4);
;         const f32x4 h0 = {bf_lo(w[j][0]) * rstd * a0[0] + b0[0], bf_hi(w[j][0]) * rstd * a0[1] + b0[1], bf_lo(w[j][1]) * rstd * a0[2] + b0[2], bf_hi(w[j][1]) * rstd * a0[3] + b0[3]};
;         const f32x4 h1 = {bf_lo(w[j][2]) * rstd * a1[0] + b1[0], bf_hi(w[j][2]) * rstd * a1[1] + b1[1], bf_lo(w[j][3]) * rstd * a1[2] + b1[2], bf_hi(w[j][3]) * rstd * a1[3] + b1[3]};
;         u32x4 o; o.x = pk2(h0[0], h0[1]); o.y = pk2(h0[2], h0[3]); o.z = pk2(h1[0], h1[1]); o.w = pk2(h1[2], h1[3]);
;         *(LAS u32x4*)(lrow + (((lane + 64 * j) ^ sw) << 4)) = o;
;         u32x2 q8; q8.x = pg8::pack4_fp8(h0, pg8::F8_SH); q8.y = pg8::pack4_fp8(h1, pg8::F8_SH); *(u32x2*)((char*)(o8row + 512 * j) + l8) = q8;
	s_waitcnt lgkmcnt(1)
	v_fma_f32 v230, v214, v230, v222
	v_fma_f32 v231, v216, v231, v224
	v_pk_mul_f32 v[232:233], v[160:161], v[240:241] op_sel_hi:[0,1]
	v_fma_f32 v214, v215, v232, v223
	v_fma_f32 v215, v217, v233, v225
	v_pk_mul_f32 v[216:217], v[160:161], v[242:243] op_sel_hi:[0,1]
	s_waitcnt lgkmcnt(0)
	v_fma_f32 v222, v218, v216, v226
	v_fma_f32 v223, v220, v217, v228
	v_pk_mul_f32 v[216:217], v[160:161], v[244:245] op_sel_hi:[0,1]
	v_fma_f32 v218, v219, v216, v227
	v_fma_f32 v219, v221, v217, v229
	v_bfe_u32 v216, v214, 16, 1
	v_add3_u32 v224, v214, v216, s54
	v_bfe_u32 v216, v230, 16, 1
	v_add3_u32 v216, v230, v216, s54
	v_lshrrev_b32_e32 v225, 16, v216
	v_cvt_pk_bf16_f32 v217, v223, v219
	v_cvt_pk_bf16_f32 v216, v222, v218
	v_med3_f32 v161, v230, s55, v210
	v_med3_f32 v164, v214, s55, v210
	v_mov_b32_e32 v220, 0
	v_cvt_pk_bf16_f32 v213, v231, v215
	v_cvt_pk_fp8_f32 v220, v161, v164
	v_med3_f32 v164, v215, s55, v210
	v_med3_f32 v214, v222, s55, v210
	v_med3_f32 v215, v218, s55, v210
	v_mov_b32_e32 v221, 0
	v_cvt_pk_fp8_f32 v221, v214, v215
	v_med3_f32 v161, v231, s55, v210
	v_cvt_pk_fp8_f32 v220, v161, v164 op_sel:[0,0,1]
	v_med3_f32 v161, v223, s55, v210
	v_med3_f32 v164, v219, s55, v210
	v_cvt_pk_fp8_f32 v221, v161, v164 op_sel:[0,0,1]
	v_mov_b32_e32 v215, v213
	v_and_or_b32 v214, v224, s52, v225
	ds_write_b128 v198, v[214:217]
	global_store_dwordx2 v[150:151], v[220:221], off offset:512
	ds_read_b128 v[214:217], v189 offset:4096
	ds_read_b128 v[218:221], v189 offset:4112
	ds_read_b128 v[222:225], v190 offset:4096
	ds_read_b128 v[226:229], v190 offset:4112
	v_pk_mul_f32 v[178:179], v[160:161], v[178:179] op_sel_hi:[0,1]
	s_waitcnt lgkmcnt(3)
	v_mov_b32_e32 v231, v216
	s_waitcnt lgkmcnt(1)
	v_mov_b32_e32 v233, v224
	v_fma_f32 v178, v178, v215, v223
	v_fma_f32 v179, v179, v217, v225
	v_mov_b32_e32 v215, v220
	s_waitcnt lgkmcnt(0)
	v_mov_b32_e32 v217, v228
	v_pk_mul_f32 v[156:157], v[160:161], v[156:157] op_sel_hi:[0,1]
	v_pk_mul_f32 v[180:181], v[160:161], v[180:181] op_sel_hi:[0,1]
	v_mov_b32_e32 v230, v214
	v_mov_b32_e32 v232, v222
	v_pk_mul_f32 v[158:159], v[160:161], v[158:159] op_sel_hi:[0,1]
	v_fma_f32 v156, v156, v219, v227
	v_fma_f32 v157, v157, v221, v229
	v_pk_fma_f32 v[180:181], v[180:181], v[230:231], v[232:233]
	v_fma_f32 v214, v158, v218, v226
	v_fma_f32 v215, v159, v215, v217
	v_bfe_u32 v161, v179, 16, 1
	v_cvt_pk_bf16_f32 v164, v180, v178
	v_bfe_u32 v216, v181, 16, 1
	v_cvt_pk_bf16_f32 v159, v215, v157
	v_cvt_pk_bf16_f32 v158, v214, v156
	v_med3_f32 v180, v180, s55, v210
	v_med3_f32 v213, v178, s55, v210
	v_mov_b32_e32 v178, 0
	v_add3_u32 v161, v179, v161, s54
	v_add3_u32 v216, v181, v216, s54
	v_cvt_pk_fp8_f32 v178, v180, v213
	v_med3_f32 v180, v181, s55, v210
	v_med3_f32 v181, v179, s55, v210
	v_med3_f32 v213, v214, s55, v210
	v_med3_f32 v156, v156, s55, v210
	v_mov_b32_e32 v179, 0
	v_cvt_pk_fp8_f32 v179, v213, v156
	v_med3_f32 v156, v215, s55, v210
	v_med3_f32 v157, v157, s55, v210
	v_cvt_pk_fp8_f32 v178, v180, v181 op_sel:[0,0,1]
	v_cvt_pk_fp8_f32 v179, v156, v157 op_sel:[0,0,1]
	v_lshrrev_b32_e32 v216, 16, v216
	v_and_or_b32 v157, v161, s52, v216
	v_mov_b32_e32 v156, v164
	ds_write_b128 v199, v[156:159]
	global_store_dwordx2 v[150:151], v[178:179], off offset:1024
	ds_read_b128 v[156:159], v189 offset:6144
	ds_read_b128 v[178:181], v189 offset:6160
	ds_read_b128 v[214:217], v190 offset:6144
	ds_read_b128 v[218:221], v190 offset:6160
	v_pk_mul_f32 v[152:153], v[160:161], v[152:153] op_sel_hi:[0,1]
	s_waitcnt lgkmcnt(3)
	v_mov_b32_e32 v223, v158
	s_waitcnt lgkmcnt(1)
	v_mov_b32_e32 v225, v216
	v_fma_f32 v152, v152, v157, v215
	v_fma_f32 v153, v153, v159, v217
	v_mov_b32_e32 v157, v180
	s_waitcnt lgkmcnt(0)
	v_mov_b32_e32 v159, v220
	v_pk_mul_f32 v[146:147], v[160:161], v[146:147] op_sel_hi:[0,1]
	v_pk_mul_f32 v[154:155], v[160:161], v[154:155] op_sel_hi:[0,1]
	v_mov_b32_e32 v222, v156
	v_mov_b32_e32 v224, v214
	v_pk_mul_f32 v[148:149], v[160:161], v[148:149] op_sel_hi:[0,1]
	v_fma_f32 v146, v146, v179, v219
	v_fma_f32 v147, v147, v181, v221
	v_pk_fma_f32 v[154:155], v[154:155], v[222:223], v[224:225]
	v_fma_f32 v156, v148, v178, v218
	v_fma_f32 v157, v149, v157, v159
	v_bfe_u32 v158, v153, 16, 1
	v_cvt_pk_bf16_f32 v159, v154, v152
	v_bfe_u32 v161, v155, 16, 1
	v_cvt_pk_bf16_f32 v149, v157, v147
	v_cvt_pk_bf16_f32 v148, v156, v146
	v_med3_f32 v154, v154, s55, v210
	v_med3_f32 v160, v152, s55, v210
	v_mov_b32_e32 v152, 0
	v_add3_u32 v158, v153, v158, s54
	v_add3_u32 v161, v155, v161, s54
	v_cvt_pk_fp8_f32 v152, v154, v160
	v_med3_f32 v154, v155, s55, v210
	v_med3_f32 v155, v153, s55, v210
	v_med3_f32 v156, v156, s55, v210
	v_med3_f32 v146, v146, s55, v210
	v_mov_b32_e32 v153, 0
	v_cvt_pk_fp8_f32 v153, v156, v146
	v_med3_f32 v146, v157, s55, v210
	v_med3_f32 v147, v147, s55, v210
	v_cvt_pk_fp8_f32 v152, v154, v155 op_sel:[0,0,1]
	v_cvt_pk_fp8_f32 v153, v146, v147 op_sel:[0,0,1]
	v_lshrrev_b32_e32 v161, 16, v161
	v_and_or_b32 v147, v158, s52, v161
	v_mov_b32_e32 v146, v159
	ds_write_b128 v200, v[146:149]
	global_store_dwordx2 v[150:151], v[152:153], off offset:1536
	s_waitcnt vmcnt(7)
	v_and_b32_e32 v233, 0xffff0000, v131
	v_and_b32_e32 v232, 0xffff0000, v130
	v_lshlrev_b32_e32 v231, 16, v131
	v_lshlrev_b32_e32 v230, 16, v130
	v_pk_mul_f32 v[152:153], v[232:233], v[232:233]
	v_and_b32_e32 v237, 0xffff0000, v133
	v_and_b32_e32 v236, 0xffff0000, v132
	v_pk_fma_f32 v[160:161], v[230:231], v[230:231], v[152:153]
	v_lshlrev_b32_e32 v235, 16, v133
	v_lshlrev_b32_e32 v234, 16, v132
	v_pk_mul_f32 v[152:153], v[236:237], v[236:237]
	s_waitcnt vmcnt(6)
; #define LAS __attribute__((address_space(3)))
; __device__ __forceinline__ unsigned pk2(float lo, float hi) { return f2bf(lo) | (f2bf(hi) << 16); }
; __device__ __forceinline__ void norm_mod_regs_lds2(const u32x4 (&w)[4], const LAS float* A, const LAS float* B, LAS unsigned char* lrow, int sw, unsigned char* o8row, int lane) {
;     float s = 0.f;
; #pragma unroll
;     for (int j = 0; j < 4; ++j) {
; #pragma unroll
;         for (int i = 0; i < 4; ++i) { const float a = bf_lo(w[j][i]), b = bf_hi(w[j][i]); s += a * a + b * b; } }
;     const float rstd = 1.f / sqrtf(wave_sum(s) * (1.f / DM) + EPS_);
;     const unsigned l8 = (unsigned)lane * 8u;
; #pragma unroll
;     for (int j = 0; j < 4; ++j) {
;         const f32x4 a0 = *(const LAS f32x4*)(A + 512 * j + 8 * lane), a1 = *(const LAS f32x4*)(A + 512 * j + 8 * lane + 4), b0 = *(const LAS f32x4*)(B + 512 * j + 8 * lane), b1 = *(const LAS f32x4*)(B + 512 * j + 8 * lane + 4);
;         const f32x4 h0 = {bf_lo(w[j][0]) * rstd * a0[0] + b0[0], bf_hi(w[j][0]) * rstd * a0[1] + b0[1], bf_lo(w[j][1]) * rstd * a0[2] + b0[2], bf_hi(w[j][1]) * rstd * a0[3] + b0[3]};
;         const f32x4 h1 = {bf_lo(w[j][2]) * rstd * a1[0] + b1[0], bf_hi(w[j][2]) * rstd * a1[1] + b1[1], bf_lo(w[j][3]) * rstd * a1[2] + b1[2], bf_hi(w[j][3]) * rstd * a1[3] + b1[3]};
;         u32x4 o; o.x = pk2(h0[0], h0[1]); o.y = pk2(h0[2], h0[3]); o.z = pk2(h1[0], h1[1]); o.w = pk2(h1[2], h1[3]);
;         *(LAS u32x4*)(lrow + (((lane + 64 * j) ^ sw) << 4)) = o;
;         u32x2 q8; q8.x = pg8::pack4_fp8(h0, pg8::F8_SH); q8.y = pg8::pack4_fp8(h1, pg8::F8_SH); *(u32x2*)((char*)(o8row + 512 * j) + l8) = q8;
	v_and_b32_e32 v241, 0xffff0000, v135
	v_pk_fma_f32 v[214:215], v[234:235], v[234:235], v[152:153]
	v_and_b32_e32 v240, 0xffff0000, v134
	v_add_f32_e32 v160, v160, v161
	v_lshlrev_b32_e32 v239, 16, v135
	v_lshlrev_b32_e32 v238, 16, v134
	v_pk_mul_f32 v[152:153], v[240:241], v[240:241]
	v_add_f32_e32 v160, v214, v160
	v_pk_fma_f32 v[216:217], v[238:239], v[238:239], v[152:153]
	v_and_b32_e32 v245, 0xffff0000, v137
	v_and_b32_e32 v244, 0xffff0000, v136
	v_add_f32_e32 v160, v215, v160
	v_lshlrev_b32_e32 v243, 16, v137
	v_lshlrev_b32_e32 v242, 16, v136
	v_pk_mul_f32 v[152:153], v[244:245], v[244:245]
	v_add_f32_e32 v160, v216, v160
	v_pk_fma_f32 v[218:219], v[242:243], v[242:243], v[152:153]
	s_waitcnt vmcnt(5)
	v_and_b32_e32 v179, 0xffff0000, v139
	v_and_b32_e32 v178, 0xffff0000, v138
	v_add_f32_e32 v160, v217, v160
	v_lshlrev_b32_e32 v181, 16, v139
	v_lshlrev_b32_e32 v180, 16, v138
	v_pk_mul_f32 v[152:153], v[178:179], v[178:179]
	v_add_f32_e32 v160, v218, v160
	v_pk_fma_f32 v[220:221], v[180:181], v[180:181], v[152:153]
	v_and_b32_e32 v157, 0xffff0000, v141
	v_and_b32_e32 v156, 0xffff0000, v140
	v_add_f32_e32 v160, v219, v160
	v_lshlrev_b32_e32 v159, 16, v141
	v_lshlrev_b32_e32 v158, 16, v140
	v_pk_mul_f32 v[152:153], v[156:157], v[156:157]
	v_add_f32_e32 v160, v220, v160
	v_pk_fma_f32 v[222:223], v[158:159], v[158:159], v[152:153]
	s_waitcnt vmcnt(4)
	v_and_b32_e32 v153, 0xffff0000, v143
	v_and_b32_e32 v152, 0xffff0000, v142
	v_add_f32_e32 v160, v221, v160
	v_lshlrev_b32_e32 v155, 16, v143
	v_lshlrev_b32_e32 v154, 16, v142
	v_pk_mul_f32 v[224:225], v[152:153], v[152:153]
	v_add_f32_e32 v160, v222, v160
	v_and_b32_e32 v147, 0xffff0000, v145
	v_and_b32_e32 v146, 0xffff0000, v144
	v_pk_fma_f32 v[224:225], v[154:155], v[154:155], v[224:225]
	v_add_f32_e32 v160, v223, v160
	v_lshlrev_b32_e32 v149, 16, v145
	v_lshlrev_b32_e32 v148, 16, v144
	v_pk_mul_f32 v[150:151], v[146:147], v[146:147]
	v_add_f32_e32 v160, v224, v160
	v_pk_fma_f32 v[150:151], v[148:149], v[148:149], v[150:151]
	v_add_f32_e32 v160, v225, v160
	v_add_f32_e32 v150, v150, v160
	v_add_f32_e32 v150, v151, v150
	ds_bpermute_b32 v151, v183, v150
	s_add_i32 s50, s24, 1
	s_ashr_i32 s51, s50, 31
	s_lshl_b64 s[22:23], s[50:51], 11
	ds_read_b128 v[214:217], v189
	ds_read_b128 v[218:221], v189 offset:16
	s_waitcnt lgkmcnt(2)
	v_add_f32_e32 v150, v150, v151
	ds_bpermute_b32 v151, v184, v150
	ds_read_b128 v[222:225], v190
	ds_read_b128 v[226:229], v190 offset:16
	s_waitcnt lgkmcnt(4)
	v_mov_b32_e32 v246, v214
	s_waitcnt lgkmcnt(3)
	v_mov_b32_e32 v214, v218
	v_mov_b32_e32 v247, v216
	s_waitcnt lgkmcnt(2)
	v_add_f32_e32 v150, v150, v151
	ds_bpermute_b32 v151, v185, v150
	v_mov_b32_e32 v216, v215
	v_mov_b32_e32 v215, v220
	v_mov_b32_e32 v220, v219
	s_waitcnt lgkmcnt(2)
	v_mov_b32_e32 v248, v222
	s_waitcnt lgkmcnt(0)
	v_add_f32_e32 v160, v150, v151
	ds_bpermute_b32 v161, v186, v160
	v_lshl_add_u64 v[150:151], v[176:177], 0, s[22:23]
	v_mov_b32_e32 v249, v224
	v_mov_b32_e32 v224, v223
	v_mov_b32_e32 v222, v226
	s_waitcnt lgkmcnt(0)
	v_add_f32_e32 v160, v160, v161
	ds_bpermute_b32 v161, v187, v160
	v_mov_b32_e32 v223, v228
	v_mov_b32_e32 v228, v227
	s_waitcnt lgkmcnt(0)
	v_add_f32_e32 v160, v160, v161
	ds_bpermute_b32 v161, v188, v160
	s_waitcnt lgkmcnt(0)
	v_add_f32_e32 v160, v160, v161
	v_fmamk_f32 v160, v160, 0x3a000000, v195
	v_mul_f32_e32 v161, 0x4f800000, v160
	v_cmp_gt_f32_e32 vcc, s53, v160
	s_nop 1
	v_cndmask_b32_e32 v160, v160, v161, vcc
	v_sqrt_f32_e32 v161, v160
	s_nop 0
	v_add_u32_e32 v164, -1, v161
	v_fma_f32 v213, -v164, v161, v160
	v_cmp_ge_f32_e64 s[22:23], 0, v213
	v_add_u32_e32 v213, 1, v161
	s_nop 0
	v_cndmask_b32_e64 v164, v161, v164, s[22:23]
	v_fma_f32 v161, -v213, v161, v160
	v_cmp_lt_f32_e64 s[22:23], 0, v161
	s_nop 1
	v_cndmask_b32_e64 v161, v164, v213, s[22:23]
	v_mul_f32_e32 v164, 0x37800000, v161
	v_cndmask_b32_e32 v161, v161, v164, vcc
	v_cmp_class_f32_e32 vcc, v160, v196
	s_nop 1
	v_cndmask_b32_e32 v160, v161, v160, vcc
	v_div_scale_f32 v161, s[22:23], v160, v160, 1.0
	v_rcp_f32_e32 v164, v161
	s_nop 0
	v_fma_f32 v213, -v161, v164, 1.0
	v_fmac_f32_e32 v164, v213, v164
	v_div_scale_f32 v213, vcc, 1.0, v160, 1.0
	v_mul_f32_e32 v218, v213, v164
	v_fma_f32 v219, -v161, v218, v213
	v_fmac_f32_e32 v218, v219, v164
	v_fma_f32 v161, -v161, v218, v213
	v_div_fmas_f32 v161, v161, v164, v218
	v_div_fixup_f32 v160, v161, v160, 1.0
	v_pk_mul_f32 v[226:227], v[160:161], v[232:233] op_sel_hi:[0,1]
	v_pk_fma_f32 v[224:225], v[216:217], v[226:227], v[224:225]
	v_pk_mul_f32 v[216:217], v[160:161], v[234:235] op_sel_hi:[0,1]
	v_pk_mul_f32 v[218:219], v[160:161], v[230:231] op_sel_hi:[0,1]
	v_pk_fma_f32 v[214:215], v[214:215], v[216:217], v[222:223]
	v_pk_mul_f32 v[216:217], v[160:161], v[236:237] op_sel_hi:[0,1]
	v_pk_fma_f32 v[218:219], v[246:247], v[218:219], v[248:249]
	v_pk_fma_f32 v[220:221], v[220:221], v[216:217], v[228:229]
	v_bfe_u32 v216, v224, 16, 1
	v_add3_u32 v222, v224, v216, s54
	v_bfe_u32 v216, v218, 16, 1
	v_bfe_u32 v217, v219, 16, 1
	v_add3_u32 v217, v219, v217, s54
	v_add3_u32 v216, v218, v216, s54
	v_lshrrev_b32_e32 v227, 16, v216
	v_lshrrev_b32_e32 v228, 16, v217
	v_cvt_pk_bf16_f32 v217, v215, v221
	v_cvt_pk_bf16_f32 v216, v214, v220
	v_med3_f32 v161, v218, s55, v210
	v_med3_f32 v164, v224, s55, v210
	v_mov_b32_e32 v218, 0
	v_cvt_pk_fp8_f32 v218, v161, v164
	v_med3_f32 v161, v219, s55, v210
	v_med3_f32 v214, v214, s55, v210
	v_med3_f32 v220, v220, s55, v210
	v_mov_b32_e32 v219, 0
	v_cvt_pk_fp8_f32 v219, v214, v220
	v_med3_f32 v164, v225, s55, v210
	v_cvt_pk_fp8_f32 v218, v161, v164 op_sel:[0,0,1]
	v_med3_f32 v161, v215, s55, v210
	v_med3_f32 v164, v221, s55, v210
	v_cvt_pk_fp8_f32 v219, v161, v164 op_sel:[0,0,1]
	v_bfe_u32 v213, v225, 16, 1
	v_add3_u32 v213, v225, v213, s54
	v_and_or_b32 v215, v213, s52, v228
	v_and_or_b32 v214, v222, s52, v227
	ds_write_b128 v201, v[214:217]
	global_store_dwordx2 v[150:151], v[218:219], off
	ds_read_b128 v[214:217], v189 offset:2048
	ds_read_b128 v[218:221], v189 offset:2064
	ds_read_b128 v[222:225], v190 offset:2048
	ds_read_b128 v[226:229], v190 offset:2064
	v_pk_mul_f32 v[230:231], v[160:161], v[238:239] op_sel_hi:[0,1]
	s_waitcnt lgkmcnt(3)
; #define LAS __attribute__((address_space(3)))
; __device__ __forceinline__ unsigned pk2(float lo, float hi) { return f2bf(lo) | (f2bf(hi) << 16); }
; __device__ __forceinline__ void norm_mod_regs_lds2(const u32x4 (&w)[4], const LAS float* A, const LAS float* B, LAS unsigned char* lrow, int sw, unsigned char* o8row, int lane) {
;     ...
;     for (int j = 0; j < 4; ++j) {
;         const f32x4 a0 = *(const LAS f32x4*)(A + 512 * j + 8 * lane), a1 = *(const LAS f32x4*)(A + 512 * j + 8 * lane + 4), b0 = *(const LAS f32x4*)(B + 512 * j + 8 * lane), b1 = *(const LAS f32x4*)(B + 512 * j + 8 * lane + 4);
;         const f32x4 h0 = {bf_lo(w[j][0]) * rstd * a0[0] + b0[0], bf_hi(w[j][0]) * rstd * a0[1] + b0[1], bf_lo(w[j][1]) * rstd * a0[2] + b0[2], bf_hi(w[j][1]) * rstd * a0[3] + b0[3]};
;         const f32x4 h1 = {bf_lo(w[j][2]) * rstd * a1[0] + b1[0], bf_hi(w[j][2]) * rstd * a1[1] + b1[1], bf_lo(w[j][3]) * rstd * a1[2] + b1[2], bf_hi(w[j][3]) * rstd * a1[3] + b1[3]};
;         u32x4 o; o.x = pk2(h0[0], h0[1]); o.y = pk2(h0[2], h0[3]); o.z = pk2(h1[0], h1[1]); o.w = pk2(h1[2], h1[3]);
;         *(LAS u32x4*)(lrow + (((lane + 64 * j) ^ sw) << 4)) = o;
;         u32x2 q8; q8.x = pg8::pack4_fp8(h0, pg8::F8_SH); q8.y = pg8::pack4_fp8(h1, pg8::F8_SH); *(u32x2*)((char*)(o8row + 512 * j) + l8) = q8;
; __device__ __forceinline__ void p9_fused4(Frame& F) {
;     ...
; #pragma unroll
;         for (int i = NFR; i < 32; ++i) fbr[i] = *(const bf16x8*)(wrb + (size_t)(i >> 2) * 4096 + (lo16 + (unsigned)((i & 3) * 1024)));
;         if (pass < 3) {
; #pragma unroll
;             for (int q = 0; q < 2; ++q)
; #pragma unroll
;                 for (int j = 0; j < 4; ++j) xw[q][j] = ldu16(WSP(bf16_t, WS_X1) + (size_t)(t0 + (pass + 1) * 16 + wave * 2 + q) * DM + 512 * j, lo16);
	s_waitcnt lgkmcnt(1)
	v_fma_f32 v230, v230, v214, v222
	v_fma_f32 v231, v231, v216, v224
	v_pk_mul_f32 v[232:233], v[160:161], v[240:241] op_sel_hi:[0,1]
	v_fma_f32 v214, v232, v215, v223
	v_fma_f32 v215, v233, v217, v225
	v_pk_mul_f32 v[216:217], v[160:161], v[242:243] op_sel_hi:[0,1]
	s_waitcnt lgkmcnt(0)
	v_fma_f32 v222, v216, v218, v226
	v_fma_f32 v223, v217, v220, v228
	v_pk_mul_f32 v[216:217], v[160:161], v[244:245] op_sel_hi:[0,1]
	v_fma_f32 v218, v216, v219, v227
	v_fma_f32 v219, v217, v221, v229
	v_bfe_u32 v216, v214, 16, 1
	v_add3_u32 v224, v214, v216, s54
	v_bfe_u32 v216, v230, 16, 1
	v_add3_u32 v216, v230, v216, s54
	v_lshrrev_b32_e32 v225, 16, v216
	v_cvt_pk_bf16_f32 v217, v223, v219
	v_cvt_pk_bf16_f32 v216, v222, v218
	v_med3_f32 v161, v230, s55, v210
	v_med3_f32 v164, v214, s55, v210
	v_mov_b32_e32 v220, 0
	v_cvt_pk_bf16_f32 v213, v231, v215
	v_cvt_pk_fp8_f32 v220, v161, v164
	v_med3_f32 v164, v215, s55, v210
	v_med3_f32 v214, v222, s55, v210
	v_med3_f32 v215, v218, s55, v210
	v_mov_b32_e32 v221, 0
	v_cvt_pk_fp8_f32 v221, v214, v215
	v_med3_f32 v161, v231, s55, v210
	v_cvt_pk_fp8_f32 v220, v161, v164 op_sel:[0,0,1]
	v_med3_f32 v161, v223, s55, v210
	v_med3_f32 v164, v219, s55, v210
	v_cvt_pk_fp8_f32 v221, v161, v164 op_sel:[0,0,1]
	v_mov_b32_e32 v215, v213
	v_and_or_b32 v214, v224, s52, v225
	ds_write_b128 v202, v[214:217]
	global_store_dwordx2 v[150:151], v[220:221], off offset:512
	ds_read_b128 v[214:217], v189 offset:4096
	ds_read_b128 v[218:221], v189 offset:4112
	ds_read_b128 v[222:225], v190 offset:4096
	ds_read_b128 v[226:229], v190 offset:4112
	v_pk_mul_f32 v[178:179], v[160:161], v[178:179] op_sel_hi:[0,1]
	s_waitcnt lgkmcnt(3)
	v_mov_b32_e32 v231, v216
	s_waitcnt lgkmcnt(1)
	v_mov_b32_e32 v233, v224
	v_fma_f32 v178, v178, v215, v223
	v_fma_f32 v179, v179, v217, v225
	v_mov_b32_e32 v215, v220
	s_waitcnt lgkmcnt(0)
	v_mov_b32_e32 v217, v228
	v_pk_mul_f32 v[156:157], v[160:161], v[156:157] op_sel_hi:[0,1]
	v_pk_mul_f32 v[180:181], v[160:161], v[180:181] op_sel_hi:[0,1]
	v_mov_b32_e32 v230, v214
	v_mov_b32_e32 v232, v222
	v_pk_mul_f32 v[158:159], v[160:161], v[158:159] op_sel_hi:[0,1]
	v_fma_f32 v156, v156, v219, v227
	v_fma_f32 v157, v157, v221, v229
	v_pk_fma_f32 v[180:181], v[180:181], v[230:231], v[232:233]
	v_fma_f32 v214, v158, v218, v226
	v_fma_f32 v215, v159, v215, v217
	v_bfe_u32 v161, v179, 16, 1
	v_cvt_pk_bf16_f32 v164, v180, v178
	v_bfe_u32 v216, v181, 16, 1
	v_cvt_pk_bf16_f32 v159, v215, v157
	v_cvt_pk_bf16_f32 v158, v214, v156
	v_med3_f32 v180, v180, s55, v210
	v_med3_f32 v213, v178, s55, v210
	v_mov_b32_e32 v178, 0
	v_add3_u32 v161, v179, v161, s54
	v_add3_u32 v216, v181, v216, s54
	v_cvt_pk_fp8_f32 v178, v180, v213
	v_med3_f32 v180, v181, s55, v210
	v_med3_f32 v181, v179, s55, v210
	v_med3_f32 v213, v214, s55, v210
	v_med3_f32 v156, v156, s55, v210
	v_mov_b32_e32 v179, 0
	v_cvt_pk_fp8_f32 v179, v213, v156
	v_med3_f32 v156, v215, s55, v210
	v_med3_f32 v157, v157, s55, v210
	v_cvt_pk_fp8_f32 v178, v180, v181 op_sel:[0,0,1]
	v_cvt_pk_fp8_f32 v179, v156, v157 op_sel:[0,0,1]
	v_lshrrev_b32_e32 v216, 16, v216
	v_and_or_b32 v157, v161, s52, v216
	v_mov_b32_e32 v156, v164
	ds_write_b128 v203, v[156:159]
	global_store_dwordx2 v[150:151], v[178:179], off offset:1024
	ds_read_b128 v[156:159], v189 offset:6144
	ds_read_b128 v[178:181], v189 offset:6160
	ds_read_b128 v[214:217], v190 offset:6144
	ds_read_b128 v[218:221], v190 offset:6160
	v_pk_mul_f32 v[152:153], v[160:161], v[152:153] op_sel_hi:[0,1]
	s_waitcnt lgkmcnt(3)
	v_mov_b32_e32 v223, v158
	s_waitcnt lgkmcnt(1)
	v_mov_b32_e32 v225, v216
	v_fma_f32 v152, v152, v157, v215
	v_fma_f32 v153, v153, v159, v217
	v_mov_b32_e32 v157, v180
	s_waitcnt lgkmcnt(0)
	v_mov_b32_e32 v159, v220
	v_pk_mul_f32 v[146:147], v[160:161], v[146:147] op_sel_hi:[0,1]
	v_pk_mul_f32 v[154:155], v[160:161], v[154:155] op_sel_hi:[0,1]
	v_mov_b32_e32 v222, v156
	v_mov_b32_e32 v224, v214
	v_pk_mul_f32 v[148:149], v[160:161], v[148:149] op_sel_hi:[0,1]
	v_fma_f32 v146, v146, v179, v219
	v_fma_f32 v147, v147, v181, v221
	v_pk_fma_f32 v[154:155], v[154:155], v[222:223], v[224:225]
	v_fma_f32 v156, v148, v178, v218
	v_fma_f32 v157, v149, v157, v159
	v_bfe_u32 v158, v153, 16, 1
	v_cvt_pk_bf16_f32 v159, v154, v152
	v_bfe_u32 v161, v155, 16, 1
	v_cvt_pk_bf16_f32 v149, v157, v147
	v_cvt_pk_bf16_f32 v148, v156, v146
	v_med3_f32 v154, v154, s55, v210
	v_med3_f32 v160, v152, s55, v210
	v_mov_b32_e32 v152, 0
	v_add3_u32 v158, v153, v158, s54
	v_add3_u32 v161, v155, v161, s54
	v_cvt_pk_fp8_f32 v152, v154, v160
	v_med3_f32 v154, v155, s55, v210
	v_med3_f32 v155, v153, s55, v210
	v_med3_f32 v156, v156, s55, v210
	v_med3_f32 v146, v146, s55, v210
	v_mov_b32_e32 v153, 0
	v_cvt_pk_fp8_f32 v153, v156, v146
	v_med3_f32 v146, v157, s55, v210
	v_med3_f32 v147, v147, s55, v210
	v_cvt_pk_fp8_f32 v152, v154, v155 op_sel:[0,0,1]
	v_cvt_pk_fp8_f32 v153, v146, v147 op_sel:[0,0,1]
	v_lshrrev_b32_e32 v161, 16, v161
	v_and_or_b32 v147, v158, s52, v161
	v_mov_b32_e32 v146, v159
	ds_write_b128 v204, v[146:149]
	global_store_dwordx2 v[150:151], v[152:153], off offset:1536
	global_load_dwordx4 v[146:149], v[168:169], off
	s_nop 0
	global_load_dwordx4 v[150:153], v[170:171], off
	global_load_dwordx4 v[154:157], v[172:173], off
	global_load_dwordx4 v[158:161], v[174:175], off
	s_cmp_lg_u32 s27, 48
	s_cbranch_scc0 .LBB0_1401
	s_add_i32 s22, s24, 16
	s_ashr_i32 s23, s22, 31
	s_lshl_b64 s[22:23], s[22:23], 12
	v_lshl_add_u64 v[126:127], v[166:167], 0, s[22:23]
	s_add_i32 s22, s24, 17
	s_ashr_i32 s23, s22, 31
	s_lshl_b64 s[22:23], s[22:23], 12
	v_lshl_add_u64 v[142:143], v[166:167], 0, s[22:23]
	global_load_dwordx4 v[114:117], v[126:127], off
	global_load_dwordx4 v[118:121], v[126:127], off offset:1024
	global_load_dwordx4 v[122:125], v[126:127], off offset:2048
	s_nop 0
	global_load_dwordx4 v[126:129], v[126:127], off offset:3072
	s_nop 0
	global_load_dwordx4 v[130:133], v[142:143], off
	global_load_dwordx4 v[134:137], v[142:143], off offset:1024
	global_load_dwordx4 v[138:141], v[142:143], off offset:2048
	s_nop 0
	global_load_dwordx4 v[142:145], v[142:143], off offset:3072
